# LayerNorm-1: row loads and gamma/beta reloads issued through a rolling window of free VGPRs (15 loads in flight instead of 2-3) on top of v24
# speedup vs baseline: 1.0185x; 1.0089x over previous
; __device__ __forceinline__ float bflo(unsigned w) { return __uint_as_float(w << 16); }
; __device__ __forceinline__ float bfhi(unsigned w) { return __uint_as_float(w & 0xffff0000u); }
; template <bool WB = true>
; __device__ __forceinline__ void ln1_phase(const bf16_t* buf, bf16_t* h1b, unsigned* xqs, float* sx, const float* gam, const float* bet, int G, int b) {
;     ...
;     for (int row0 = gw; row0 < S_; row0 += R * NGW) {
;         f32x4 v[R][8]; float sum[R], sq[R], amax[R];
; #pragma unroll
;         for (int q = 0; q < R; ++q) {
;             const int row = min(row0 + q * NGW, S_ - 1);
;             const bf16_t* rp = buf + (size_t)row * D_;
;             sum[q] = 0.f;
; #pragma unroll
;             for (int j = 0; j < 8; ++j) { const u32x2 w = *(const u32x2*)(rp + 256 * j + 4 * lane); v[q][j] = (f32x4){bflo(w.x), bfhi(w.x), bflo(w.y), bfhi(w.y)}; sum[q] += (v[q][j].x + v[q][j].y) + (v[q][j].z + v[q][j].w); }
;         }
; #pragma unroll
;         for (int q = 0; q < R; ++q) sum[q] = wave_sum(sum[q]) * (1.0f / D_);
.LBB0_543:
	v_mbcnt_lo_u32_b32 v219, -1, 0
	v_mbcnt_hi_u32_b32 v219, -1, v219
	s_add_u32 s30, s92, 0x17800000
	s_addc_u32 s31, s93, 0
	v_lshlrev_b32_e32 v219, 3, v219
	s_lshl_b32 s20, s4, 12
	s_add_u32 s20, s30, s20
	s_addc_u32 s21, s31, 0
	s_add_i32 s22, s62, s4
	s_min_i32 s22, s22, 0x3fff
	s_lshl_b32 s22, s22, 12
	s_add_u32 s22, s30, s22
	s_addc_u32 s23, s31, 0
	s_add_i32 s24, s5, s4
	s_min_i32 s24, s24, 0x3fff
	s_lshl_b32 s24, s24, 12
	s_add_u32 s24, s30, s24
	s_addc_u32 s25, s31, 0
	s_mul_i32 s26, s96, 24
	s_add_i32 s26, s26, s4
	s_min_i32 s26, s26, 0x3fff
	s_lshl_b32 s26, s26, 12
	s_add_u32 s26, s30, s26
	s_addc_u32 s27, s31, 0
	global_load_dwordx2 v[224:225], v219, s[20:21]
	global_load_dwordx2 v[226:227], v219, s[20:21] offset:512
	global_load_dwordx2 v[228:229], v219, s[20:21] offset:3584
	global_load_dwordx2 v[230:231], v219, s[20:21] offset:1536
	global_load_dwordx2 v[232:233], v219, s[20:21] offset:1024
	global_load_dwordx2 v[234:235], v219, s[20:21] offset:2048
	global_load_dwordx2 v[236:237], v219, s[20:21] offset:2560
	global_load_dwordx2 v[238:239], v219, s[20:21] offset:3072
	global_load_dwordx2 v[240:241], v219, s[22:23]
	global_load_dwordx2 v[244:245], v219, s[22:23] offset:512
	global_load_dwordx2 v[246:247], v219, s[22:23] offset:3584
	global_load_dwordx2 v[248:249], v219, s[22:23] offset:1536
	global_load_dwordx2 v[250:251], v219, s[22:23] offset:1024
	global_load_dwordx2 v[252:253], v219, s[22:23] offset:2048
	global_load_dwordx2 v[254:255], v219, s[22:23] offset:2560
	v_lshl_add_u64 v[44:45], s[92:93], 0, v[38:39]
	s_waitcnt vmcnt(14)
	v_mov_b64_e32 v[2:3], v[224:225]
	global_load_dwordx2 v[224:225], v219, s[22:23] offset:3072
	s_waitcnt vmcnt(14)
	v_mov_b64_e32 v[4:5], v[226:227]
	global_load_dwordx2 v[226:227], v219, s[24:25]
	s_add_i32 s56, s62, s4
	s_min_i32 s0, s56, 0x3fff
	s_ashr_i32 s1, s0, 31
	s_lshl_b64 s[0:1], s[0:1], 12
	s_add_i32 s58, s5, s4
	s_waitcnt vmcnt(14)
	v_mov_b64_e32 v[50:51], v[228:229]
	global_load_dwordx2 v[228:229], v219, s[24:25] offset:512
	v_lshlrev_b32_e32 v140, 16, v2
	v_lshlrev_b32_e32 v141, 16, v4
	v_and_b32_e32 v143, 0xffff0000, v4
	v_and_b32_e32 v142, 0xffff0000, v2
	v_lshlrev_b32_e32 v137, 16, v5
	v_lshlrev_b32_e32 v136, 16, v3
	v_and_b32_e32 v139, 0xffff0000, v5
	v_and_b32_e32 v138, 0xffff0000, v3
	v_pk_add_f32 v[2:3], v[140:141], v[142:143]
	v_pk_add_f32 v[4:5], v[136:137], v[138:139]
	v_lshlrev_b32_e32 v43, 16, v51
	v_pk_add_f32 v[2:3], v[2:3], v[4:5]
	s_waitcnt vmcnt(14)
	v_mov_b64_e32 v[4:5], v[230:231]
	global_load_dwordx2 v[230:231], v219, s[24:25] offset:3584
	v_add_f32_e32 v2, 0, v2
	v_add_f32_e32 v8, v2, v3
	s_waitcnt vmcnt(14)
	v_mov_b64_e32 v[2:3], v[232:233]
	global_load_dwordx2 v[232:233], v219, s[24:25] offset:1536
	v_and_b32_e32 v41, 0xffff0000, v51
	v_lshlrev_b32_e32 v64, 16, v4
	v_and_b32_e32 v65, 0xffff0000, v4
	v_lshlrev_b32_e32 v66, 16, v5
	v_and_b32_e32 v67, 0xffff0000, v5
	s_waitcnt vmcnt(14)
	v_mov_b64_e32 v[4:5], v[234:235]
	global_load_dwordx2 v[234:235], v219, s[24:25] offset:1024
	v_lshlrev_b32_e32 v77, 16, v3
	v_lshlrev_b32_e32 v76, 16, v2
	v_and_b32_e32 v145, 0xffff0000, v3
	v_and_b32_e32 v144, 0xffff0000, v2
	v_pk_add_f32 v[2:3], v[76:77], v[144:145]
	v_add_f32_e32 v58, v64, v65
	v_pk_add_f32 v[2:3], v[2:3], v[2:3] op_sel:[0,1] op_sel_hi:[1,0]
	v_add_f32_e32 v56, v66, v67
	v_and_b32_e32 v61, 0xffff0000, v4
	s_waitcnt lgkmcnt(0)
	v_lshlrev_b32_e32 v9, 16, v4
	v_lshlrev_b32_e32 v59, 16, v5
	v_and_b32_e32 v57, 0xffff0000, v5
	v_mov_b32_e32 v3, v61
	v_pk_add_f32 v[2:3], v[8:9], v[2:3]
	v_pk_add_f32 v[4:5], v[58:59], v[56:57]
	s_nop 0
	v_pk_add_f32 v[46:47], v[2:3], v[4:5]
	s_waitcnt vmcnt(14)
	v_mov_b64_e32 v[2:3], v[236:237]
	global_load_dwordx2 v[236:237], v219, s[24:25] offset:2048
	s_waitcnt vmcnt(14)
	v_mov_b64_e32 v[4:5], v[238:239]
	global_load_dwordx2 v[238:239], v219, s[24:25] offset:2560
	v_lshlrev_b32_e32 v44, 16, v50
	v_and_b32_e32 v45, 0xffff0000, v50
	v_pk_add_f32 v[46:47], v[46:47], v[46:47] op_sel:[0,1] op_sel_hi:[1,0]
	v_lshl_add_u64 v[50:51], v[12:13], 0, s[0:1]
	v_mov_b32_e32 v47, v44
	s_min_i32 s0, s58, 0x3fff
	s_ashr_i32 s1, s0, 31
	s_lshl_b64 s[0:1], s[0:1], 12
	v_lshlrev_b32_e32 v7, 16, v3
	v_lshlrev_b32_e32 v6, 16, v2
	v_and_b32_e32 v147, 0xffff0000, v3
	v_and_b32_e32 v146, 0xffff0000, v2
	v_pk_add_f32 v[48:49], v[6:7], v[146:147]
	v_lshlrev_b32_e32 v2, 16, v4
	v_and_b32_e32 v3, 0xffff0000, v4
	v_lshlrev_b32_e32 v4, 16, v5
	v_and_b32_e32 v5, 0xffff0000, v5
	v_pk_add_f32 v[48:49], v[48:49], v[48:49] op_sel:[0,1] op_sel_hi:[1,0]
	v_add_f32_e32 v42, v2, v3
	v_add_f32_e32 v40, v4, v5
	v_mov_b32_e32 v49, v45
	v_pk_add_f32 v[46:47], v[46:47], v[48:49]
	v_pk_add_f32 v[48:49], v[42:43], v[40:41]
	s_nop 0
	v_pk_add_f32 v[46:47], v[46:47], v[48:49]
	s_nop 0
	v_add_f32_e32 v8, v46, v47
	s_waitcnt vmcnt(14)
	v_mov_b64_e32 v[46:47], v[240:241]
	global_load_dwordx2 v[240:241], v219, s[24:25] offset:3072
	s_waitcnt vmcnt(14)
	v_mov_b64_e32 v[48:49], v[244:245]
	global_load_dwordx2 v[244:245], v219, s[26:27]
	s_waitcnt vmcnt(14)
	v_mov_b64_e32 v[82:83], v[246:247]
	global_load_dwordx2 v[246:247], v219, s[26:27] offset:512
	v_lshlrev_b32_e32 v156, 16, v46
	v_lshlrev_b32_e32 v157, 16, v48
	v_and_b32_e32 v159, 0xffff0000, v48
	v_and_b32_e32 v158, 0xffff0000, v46
	v_lshlrev_b32_e32 v153, 16, v49
	v_lshlrev_b32_e32 v152, 16, v47
	v_and_b32_e32 v155, 0xffff0000, v49
	v_and_b32_e32 v154, 0xffff0000, v47
	v_pk_add_f32 v[46:47], v[156:157], v[158:159]
	v_pk_add_f32 v[48:49], v[152:153], v[154:155]
	s_nop 0
	v_pk_add_f32 v[46:47], v[46:47], v[48:49]
	s_waitcnt vmcnt(14)
; __device__ __forceinline__ float bflo(unsigned w) { return __uint_as_float(w << 16); }
; __device__ __forceinline__ float bfhi(unsigned w) { return __uint_as_float(w & 0xffff0000u); }
; template <bool WB = true>
; __device__ __forceinline__ void ln1_phase(const bf16_t* buf, bf16_t* h1b, unsigned* xqs, float* sx, const float* gam, const float* bet, int G, int b) {
;     ...
;         for (int q = 0; q < R; ++q) {
;             const int row = min(row0 + q * NGW, S_ - 1);
;             const bf16_t* rp = buf + (size_t)row * D_;
;             sum[q] = 0.f;
; #pragma unroll
;             for (int j = 0; j < 8; ++j) { const u32x2 w = *(const u32x2*)(rp + 256 * j + 4 * lane); v[q][j] = (f32x4){bflo(w.x), bfhi(w.x), bflo(w.y), bfhi(w.y)}; sum[q] += (v[q][j].x + v[q][j].y) + (v[q][j].z + v[q][j].w); }
;         }
; #pragma unroll
;         for (int q = 0; q < R; ++q) sum[q] = wave_sum(sum[q]) * (1.0f / D_);
; #pragma unroll
;         for (int q = 0; q < R; ++q) { sq[q] = 0.f;
; #pragma unroll
;             for (int j = 0; j < 8; ++j) { v[q][j] = v[q][j] - sum[q]; sq[q] += (v[q][j].x * v[q][j].x + v[q][j].y * v[q][j].y) + (v[q][j].z * v[q][j].z + v[q][j].w * v[q][j].w); } }
	v_mov_b64_e32 v[48:49], v[248:249]
	global_load_dwordx2 v[248:249], v219, s[26:27] offset:3584
	v_add_f32_e32 v10, 0, v46
	v_add_f32_e32 v68, v10, v47
	s_waitcnt vmcnt(14)
	v_mov_b64_e32 v[46:47], v[250:251]
	global_load_dwordx2 v[250:251], v219, s[26:27] offset:1536
	v_lshlrev_b32_e32 v84, 16, v48
	v_and_b32_e32 v85, 0xffff0000, v48
	v_lshlrev_b32_e32 v86, 16, v49
	v_and_b32_e32 v87, 0xffff0000, v49
	s_waitcnt vmcnt(14)
	v_mov_b64_e32 v[48:49], v[252:253]
	global_load_dwordx2 v[252:253], v219, s[26:27] offset:1024
	v_lshlrev_b32_e32 v89, 16, v47
	v_lshlrev_b32_e32 v88, 16, v46
	v_and_b32_e32 v151, 0xffff0000, v47
	v_and_b32_e32 v150, 0xffff0000, v46
	v_pk_add_f32 v[46:47], v[88:89], v[150:151]
	v_add_f32_e32 v72, v84, v85
	v_pk_add_f32 v[46:47], v[46:47], v[46:47] op_sel:[0,1] op_sel_hi:[1,0]
	v_add_f32_e32 v70, v86, v87
	v_and_b32_e32 v75, 0xffff0000, v48
	v_lshlrev_b32_e32 v69, 16, v48
	v_lshlrev_b32_e32 v73, 16, v49
	v_and_b32_e32 v71, 0xffff0000, v49
	v_mov_b32_e32 v47, v75
	v_pk_add_f32 v[46:47], v[68:69], v[46:47]
	v_pk_add_f32 v[48:49], v[72:73], v[70:71]
	s_nop 0
	v_pk_add_f32 v[78:79], v[46:47], v[48:49]
	s_waitcnt vmcnt(14)
	v_mov_b64_e32 v[46:47], v[254:255]
	global_load_dwordx2 v[254:255], v219, s[26:27] offset:2048
	v_pk_add_f32 v[78:79], v[78:79], v[78:79] op_sel:[0,1] op_sel_hi:[1,0]
	v_lshlrev_b32_e32 v49, 16, v83
	v_lshlrev_b32_e32 v63, 16, v47
	v_lshlrev_b32_e32 v62, 16, v46
	v_and_b32_e32 v149, 0xffff0000, v47
	v_and_b32_e32 v148, 0xffff0000, v46
	s_waitcnt vmcnt(14)
	v_mov_b64_e32 v[46:47], v[224:225]
	global_load_dwordx2 v[224:225], v219, s[26:27] offset:2560
	v_pk_add_f32 v[80:81], v[62:63], v[148:149]
	v_lshlrev_b32_e32 v50, 16, v82
	v_and_b32_e32 v51, 0xffff0000, v82
	v_pk_add_f32 v[80:81], v[80:81], v[80:81] op_sel:[0,1] op_sel_hi:[1,0]
	v_mov_b32_e32 v79, v50
	v_mov_b32_e32 v81, v51
	v_pk_add_f32 v[78:79], v[78:79], v[80:81]
	v_lshlrev_b32_e32 v52, 16, v46
	v_and_b32_e32 v53, 0xffff0000, v46
	v_lshlrev_b32_e32 v54, 16, v47
	v_and_b32_e32 v55, 0xffff0000, v47
	v_add_f32_e32 v48, v52, v53
	v_add_f32_e32 v46, v54, v55
	v_and_b32_e32 v47, 0xffff0000, v83
	v_pk_add_f32 v[80:81], v[48:49], v[46:47]
	v_lshl_add_u64 v[82:83], v[12:13], 0, s[0:1]
	v_pk_add_f32 v[78:79], v[78:79], v[80:81]
	s_mul_i32 s0, s96, 24
	v_add_f32_e32 v10, v78, v79
	s_waitcnt vmcnt(14)
	v_mov_b64_e32 v[78:79], v[226:227]
	global_load_dwordx2 v[226:227], v219, s[26:27] offset:3072
	s_waitcnt vmcnt(14)
	v_mov_b64_e32 v[80:81], v[228:229]
	s_add_i32 s60, s0, s4
	s_min_i32 s0, s60, 0x3fff
	s_ashr_i32 s1, s0, 31
	s_lshl_b64 s[0:1], s[0:1], 12
	ds_bpermute_b32 v46, v167, v8
	s_waitcnt vmcnt(13)
	v_mov_b64_e32 v[100:101], v[230:231]
	s_waitcnt lgkmcnt(0)
	v_add_f32_e32 v8, v8, v46
	ds_bpermute_b32 v46, v169, v8
	s_waitcnt lgkmcnt(0)
	v_add_f32_e32 v8, v8, v46
	ds_bpermute_b32 v46, v213, v8
	s_waitcnt lgkmcnt(0)
	v_add_f32_e32 v8, v8, v46
	ds_bpermute_b32 v46, v214, v8
	s_waitcnt lgkmcnt(0)
	v_add_f32_e32 v8, v8, v46
	ds_bpermute_b32 v46, v215, v8
	s_waitcnt lgkmcnt(0)
	v_add_f32_e32 v8, v8, v46
	ds_bpermute_b32 v46, v216, v8
	s_waitcnt lgkmcnt(0)
	v_add_f32_e32 v56, v8, v46
	ds_bpermute_b32 v8, v167, v10
	v_fmac_f32_e32 v142, 0xba000000, v56
	v_fmac_f32_e32 v143, 0xba000000, v56
	v_fmac_f32_e32 v138, 0xba000000, v56
	v_fmac_f32_e32 v140, 0xba000000, v56
	s_waitcnt lgkmcnt(0)
	v_add_f32_e32 v8, v10, v8
	ds_bpermute_b32 v10, v169, v8
	v_fmac_f32_e32 v139, 0xba000000, v56
	v_fmac_f32_e32 v141, 0xba000000, v56
	v_mov_b32_e32 v185, v142
	v_fmac_f32_e32 v136, 0xba000000, v56
	s_waitcnt lgkmcnt(0)
	v_add_f32_e32 v8, v8, v10
	ds_bpermute_b32 v10, v213, v8
	v_fmac_f32_e32 v137, 0xba000000, v56
	v_mov_b32_e32 v184, v140
	v_fmac_f32_e32 v144, 0xba000000, v56
	v_fmac_f32_e32 v145, 0xba000000, v56
	s_waitcnt lgkmcnt(0)
	v_add_f32_e32 v8, v8, v10
	ds_bpermute_b32 v10, v214, v8
	v_fmac_f32_e32 v77, 0xba000000, v56
	v_fmac_f32_e32 v76, 0xba000000, v56
	v_fmac_f32_e32 v64, 0xba000000, v56
	v_fmac_f32_e32 v65, 0xba000000, v56
	s_waitcnt lgkmcnt(0)
	v_add_f32_e32 v8, v8, v10
	ds_bpermute_b32 v10, v215, v8
	v_fmac_f32_e32 v66, 0xba000000, v56
	v_fmac_f32_e32 v67, 0xba000000, v56
	v_fmac_f32_e32 v57, 0xba000000, v56
	v_fmac_f32_e32 v59, 0xba000000, v56
	s_waitcnt lgkmcnt(0)
	v_add_f32_e32 v8, v8, v10
	ds_bpermute_b32 v10, v216, v8
	v_fmac_f32_e32 v61, 0xba000000, v56
	v_fmac_f32_e32 v9, 0xba000000, v56
	v_fmac_f32_e32 v146, 0xba000000, v56
	v_fmac_f32_e32 v147, 0xba000000, v56
	s_waitcnt lgkmcnt(0)
	v_add_f32_e32 v48, v8, v10
	v_fmac_f32_e32 v7, 0xba000000, v56
	v_fmac_f32_e32 v6, 0xba000000, v56
	v_lshlrev_b32_e32 v164, 16, v78
	v_lshlrev_b32_e32 v165, 16, v80
	v_and_b32_e32 v171, 0xffff0000, v80
	v_and_b32_e32 v170, 0xffff0000, v78
	v_lshlrev_b32_e32 v161, 16, v81
	v_lshlrev_b32_e32 v160, 16, v79
	v_and_b32_e32 v163, 0xffff0000, v81
	v_and_b32_e32 v162, 0xffff0000, v79
	v_pk_add_f32 v[78:79], v[164:165], v[170:171]
	v_pk_add_f32 v[80:81], v[160:161], v[162:163]
	v_fmac_f32_e32 v2, 0xba000000, v56
	v_pk_add_f32 v[78:79], v[78:79], v[80:81]
	s_waitcnt vmcnt(12)
	v_mov_b64_e32 v[80:81], v[232:233]
	v_add_f32_e32 v40, 0, v78
	v_add_f32_e32 v90, v40, v79
	s_waitcnt vmcnt(11)
; __device__ __forceinline__ float bflo(unsigned w) { return __uint_as_float(w << 16); }
; __device__ __forceinline__ float bfhi(unsigned w) { return __uint_as_float(w & 0xffff0000u); }
; template <bool WB = true>
; __device__ __forceinline__ void ln1_phase(const bf16_t* buf, bf16_t* h1b, unsigned* xqs, float* sx, const float* gam, const float* bet, int G, int b) {
;     ...
;         for (int q = 0; q < R; ++q) {
;             const int row = min(row0 + q * NGW, S_ - 1);
;             const bf16_t* rp = buf + (size_t)row * D_;
;             sum[q] = 0.f;
; #pragma unroll
;             for (int j = 0; j < 8; ++j) { const u32x2 w = *(const u32x2*)(rp + 256 * j + 4 * lane); v[q][j] = (f32x4){bflo(w.x), bfhi(w.x), bflo(w.y), bfhi(w.y)}; sum[q] += (v[q][j].x + v[q][j].y) + (v[q][j].z + v[q][j].w); }
;         }
; #pragma unroll
;         for (int q = 0; q < R; ++q) sum[q] = wave_sum(sum[q]) * (1.0f / D_);
; #pragma unroll
;         for (int q = 0; q < R; ++q) { sq[q] = 0.f;
; #pragma unroll
;             for (int j = 0; j < 8; ++j) { v[q][j] = v[q][j] - sum[q]; sq[q] += (v[q][j].x * v[q][j].x + v[q][j].y * v[q][j].y) + (v[q][j].z * v[q][j].z + v[q][j].w * v[q][j].w); } }
	v_mov_b64_e32 v[78:79], v[234:235]
	v_fmac_f32_e32 v3, 0xba000000, v56
	v_fmac_f32_e32 v4, 0xba000000, v56
	v_fmac_f32_e32 v5, 0xba000000, v56
	v_fmac_f32_e32 v41, 0xba000000, v56
	v_fmac_f32_e32 v43, 0xba000000, v56
	v_fmac_f32_e32 v45, 0xba000000, v56
	v_fmac_f32_e32 v44, 0xba000000, v56
	v_fmac_f32_e32 v154, 0xba000000, v48
	v_fmac_f32_e32 v152, 0xba000000, v48
	v_fmac_f32_e32 v158, 0xba000000, v48
	v_fmac_f32_e32 v156, 0xba000000, v48
	v_fmac_f32_e32 v155, 0xba000000, v48
	v_fmac_f32_e32 v153, 0xba000000, v48
	v_fmac_f32_e32 v159, 0xba000000, v48
	v_fmac_f32_e32 v157, 0xba000000, v48
	v_fmac_f32_e32 v150, 0xba000000, v48
	v_fmac_f32_e32 v88, 0xba000000, v48
	v_fmac_f32_e32 v151, 0xba000000, v48
	v_fmac_f32_e32 v89, 0xba000000, v48
	v_fmac_f32_e32 v85, 0xba000000, v48
	v_fmac_f32_e32 v84, 0xba000000, v48
	v_fmac_f32_e32 v87, 0xba000000, v48
	v_fmac_f32_e32 v86, 0xba000000, v48
	v_fmac_f32_e32 v71, 0xba000000, v48
	v_fmac_f32_e32 v73, 0xba000000, v48
	v_fmac_f32_e32 v75, 0xba000000, v48
	v_fmac_f32_e32 v69, 0xba000000, v48
	v_fmac_f32_e32 v148, 0xba000000, v48
	v_fmac_f32_e32 v62, 0xba000000, v48
	v_fmac_f32_e32 v149, 0xba000000, v48
	v_fmac_f32_e32 v63, 0xba000000, v48
	v_fmac_f32_e32 v53, 0xba000000, v48
	v_fmac_f32_e32 v52, 0xba000000, v48
	v_fmac_f32_e32 v55, 0xba000000, v48
	v_fmac_f32_e32 v54, 0xba000000, v48
	v_fmac_f32_e32 v47, 0xba000000, v48
	v_fmac_f32_e32 v49, 0xba000000, v48
	v_fmac_f32_e32 v51, 0xba000000, v48
	v_fmac_f32_e32 v50, 0xba000000, v48
	v_mov_b32_e32 v186, v89
	v_mov_b32_e32 v187, v151
	v_mov_b32_e32 v89, v150
	v_pk_mul_f32 v[150:151], v[88:89], v[88:89]
	v_mov_b32_e32 v74, v69
	v_mov_b32_e32 v70, v73
	v_lshlrev_b32_e32 v112, 16, v80
	v_and_b32_e32 v113, 0xffff0000, v80
	v_lshlrev_b32_e32 v114, 16, v81
	v_and_b32_e32 v115, 0xffff0000, v81
	s_waitcnt vmcnt(10)
	v_mov_b64_e32 v[80:81], v[236:237]
	v_lshlrev_b32_e32 v105, 16, v79
	v_lshlrev_b32_e32 v104, 16, v78
	v_and_b32_e32 v173, 0xffff0000, v79
	v_and_b32_e32 v172, 0xffff0000, v78
	v_pk_add_f32 v[78:79], v[104:105], v[172:173]
	v_add_f32_e32 v108, v112, v113
	v_pk_add_f32 v[78:79], v[78:79], v[78:79] op_sel:[0,1] op_sel_hi:[1,0]
	v_add_f32_e32 v106, v114, v115
	v_and_b32_e32 v111, 0xffff0000, v80
	v_lshlrev_b32_e32 v91, 16, v80
	v_lshlrev_b32_e32 v109, 16, v81
	v_and_b32_e32 v107, 0xffff0000, v81
	v_mov_b32_e32 v79, v111
	v_pk_add_f32 v[78:79], v[90:91], v[78:79]
	v_pk_add_f32 v[80:81], v[108:109], v[106:107]
	s_nop 0
	v_pk_add_f32 v[96:97], v[78:79], v[80:81]
	s_waitcnt vmcnt(9)
	v_mov_b64_e32 v[78:79], v[238:239]
	v_pk_add_f32 v[96:97], v[96:97], v[96:97] op_sel:[0,1] op_sel_hi:[1,0]
	v_lshlrev_b32_e32 v81, 16, v101
	v_lshlrev_b32_e32 v103, 16, v79
	v_lshlrev_b32_e32 v102, 16, v78
	v_and_b32_e32 v175, 0xffff0000, v79
	v_and_b32_e32 v174, 0xffff0000, v78
	s_waitcnt vmcnt(8)
	v_mov_b64_e32 v[78:79], v[240:241]
	v_pk_add_f32 v[98:99], v[102:103], v[174:175]
	v_lshlrev_b32_e32 v82, 16, v100
	v_and_b32_e32 v83, 0xffff0000, v100
	v_pk_add_f32 v[98:99], v[98:99], v[98:99] op_sel:[0,1] op_sel_hi:[1,0]
	v_mov_b32_e32 v97, v82
	v_mov_b32_e32 v99, v83
	v_pk_add_f32 v[96:97], v[96:97], v[98:99]
	v_lshlrev_b32_e32 v92, 16, v78
	v_and_b32_e32 v93, 0xffff0000, v78
	v_lshlrev_b32_e32 v94, 16, v79
	v_and_b32_e32 v95, 0xffff0000, v79
	v_add_f32_e32 v80, v92, v93
	v_add_f32_e32 v78, v94, v95
	v_and_b32_e32 v79, 0xffff0000, v101
	v_pk_add_f32 v[98:99], v[80:81], v[78:79]
	v_lshl_add_u64 v[100:101], v[12:13], 0, s[0:1]
	v_pk_add_f32 v[96:97], v[96:97], v[98:99]
	s_nop 0
	v_add_f32_e32 v40, v96, v97
	s_waitcnt vmcnt(7)
	v_mov_b64_e32 v[96:97], v[244:245]
	s_waitcnt vmcnt(6)
	v_mov_b64_e32 v[98:99], v[246:247]
	s_waitcnt vmcnt(5)
	v_mov_b64_e32 v[182:183], v[248:249]
	ds_bpermute_b32 v8, v167, v40
	s_waitcnt lgkmcnt(0)
	v_add_f32_e32 v8, v40, v8
	ds_bpermute_b32 v10, v169, v8
	s_waitcnt lgkmcnt(0)
	v_add_f32_e32 v8, v8, v10
	ds_bpermute_b32 v10, v213, v8
	s_waitcnt lgkmcnt(0)
	v_add_f32_e32 v8, v8, v10
	ds_bpermute_b32 v10, v214, v8
	s_waitcnt lgkmcnt(0)
	v_add_f32_e32 v8, v8, v10
	ds_bpermute_b32 v10, v215, v8
	s_waitcnt lgkmcnt(0)
	v_add_f32_e32 v8, v8, v10
	ds_bpermute_b32 v10, v216, v8
	s_waitcnt lgkmcnt(0)
	v_add_f32_e32 v8, v8, v10
	v_fmac_f32_e32 v162, 0xba000000, v8
	v_fmac_f32_e32 v170, 0xba000000, v8
	v_fmac_f32_e32 v163, 0xba000000, v8
	v_fmac_f32_e32 v171, 0xba000000, v8
	v_fmac_f32_e32 v160, 0xba000000, v8
	v_fmac_f32_e32 v164, 0xba000000, v8
	v_fmac_f32_e32 v161, 0xba000000, v8
	v_fmac_f32_e32 v165, 0xba000000, v8
	v_fmac_f32_e32 v172, 0xba000000, v8
	v_fmac_f32_e32 v173, 0xba000000, v8
	v_fmac_f32_e32 v105, 0xba000000, v8
	v_fmac_f32_e32 v104, 0xba000000, v8
	v_fmac_f32_e32 v112, 0xba000000, v8
	v_fmac_f32_e32 v113, 0xba000000, v8
	v_fmac_f32_e32 v114, 0xba000000, v8
	v_fmac_f32_e32 v115, 0xba000000, v8
	v_fmac_f32_e32 v107, 0xba000000, v8
	v_fmac_f32_e32 v109, 0xba000000, v8
	v_fmac_f32_e32 v111, 0xba000000, v8
	v_fmac_f32_e32 v91, 0xba000000, v8
	v_fmac_f32_e32 v174, 0xba000000, v8
	v_fmac_f32_e32 v175, 0xba000000, v8
	v_fmac_f32_e32 v103, 0xba000000, v8
	v_fmac_f32_e32 v102, 0xba000000, v8
	v_fmac_f32_e32 v92, 0xba000000, v8
	v_fmac_f32_e32 v93, 0xba000000, v8
	v_fmac_f32_e32 v94, 0xba000000, v8
	v_fmac_f32_e32 v95, 0xba000000, v8
	v_fmac_f32_e32 v79, 0xba000000, v8
	v_fmac_f32_e32 v81, 0xba000000, v8
	v_fmac_f32_e32 v83, 0xba000000, v8
	v_fmac_f32_e32 v82, 0xba000000, v8
	v_mov_b32_e32 v110, v91
	v_mov_b32_e32 v106, v109
	v_mov_b32_e32 v78, v81
	v_lshlrev_b32_e32 v190, 16, v96
	v_lshlrev_b32_e32 v191, 16, v98
	v_and_b32_e32 v193, 0xffff0000, v98
	v_and_b32_e32 v192, 0xffff0000, v96
	v_lshlrev_b32_e32 v179, 16, v99
	v_lshlrev_b32_e32 v178, 16, v97
	v_and_b32_e32 v189, 0xffff0000, v99
	v_and_b32_e32 v188, 0xffff0000, v97
	v_pk_add_f32 v[96:97], v[190:191], v[192:193]
	v_pk_add_f32 v[98:99], v[178:179], v[188:189]
	s_nop 0
	v_pk_add_f32 v[96:97], v[96:97], v[98:99]
	s_waitcnt vmcnt(4)
; __device__ __forceinline__ float bflo(unsigned w) { return __uint_as_float(w << 16); }
; __device__ __forceinline__ float bfhi(unsigned w) { return __uint_as_float(w & 0xffff0000u); }
; template <bool WB = true>
; __device__ __forceinline__ void ln1_phase(const bf16_t* buf, bf16_t* h1b, unsigned* xqs, float* sx, const float* gam, const float* bet, int G, int b) {
;     ...
;         for (int q = 0; q < R; ++q) {
;             const int row = min(row0 + q * NGW, S_ - 1);
;             const bf16_t* rp = buf + (size_t)row * D_;
;             sum[q] = 0.f;
; #pragma unroll
;             for (int j = 0; j < 8; ++j) { const u32x2 w = *(const u32x2*)(rp + 256 * j + 4 * lane); v[q][j] = (f32x4){bflo(w.x), bfhi(w.x), bflo(w.y), bfhi(w.y)}; sum[q] += (v[q][j].x + v[q][j].y) + (v[q][j].z + v[q][j].w); }
;         }
; #pragma unroll
;         for (int q = 0; q < R; ++q) sum[q] = wave_sum(sum[q]) * (1.0f / D_);
; #pragma unroll
;         for (int q = 0; q < R; ++q) { sq[q] = 0.f;
; #pragma unroll
;             for (int j = 0; j < 8; ++j) { v[q][j] = v[q][j] - sum[q]; sq[q] += (v[q][j].x * v[q][j].x + v[q][j].y * v[q][j].y) + (v[q][j].z * v[q][j].z + v[q][j].w * v[q][j].w); } }
; #pragma unroll
;         for (int q = 0; q < R; ++q) sq[q] = 1.0f / sqrtf(wave_sum(sq[q]) * (1.0f / D_) + LN_EPS);
;     ...
;         for (int j = 0; j < 8; ++j) {
;             const f32x4 gg = *(const f32x4*)(gam + 256 * j + 4 * lane), bb = *(const f32x4*)(bet + 256 * j + 4 * lane);
	v_mov_b64_e32 v[98:99], v[250:251]
	v_add_f32_e32 v42, 0, v96
	v_add_f32_e32 v120, v42, v97
	s_waitcnt vmcnt(3)
	v_mov_b64_e32 v[96:97], v[252:253]
	v_lshlrev_b32_e32 v130, 16, v98
	v_and_b32_e32 v131, 0xffff0000, v98
	v_lshlrev_b32_e32 v132, 16, v99
	v_and_b32_e32 v133, 0xffff0000, v99
	s_waitcnt vmcnt(2)
	v_mov_b64_e32 v[98:99], v[254:255]
	v_lshlrev_b32_e32 v135, 16, v97
	v_lshlrev_b32_e32 v134, 16, v96
	v_and_b32_e32 v195, 0xffff0000, v97
	v_and_b32_e32 v194, 0xffff0000, v96
	v_pk_add_f32 v[96:97], v[134:135], v[194:195]
	v_add_f32_e32 v126, v130, v131
	v_pk_add_f32 v[96:97], v[96:97], v[96:97] op_sel:[0,1] op_sel_hi:[1,0]
	v_add_f32_e32 v124, v132, v133
	v_and_b32_e32 v129, 0xffff0000, v98
	v_lshlrev_b32_e32 v121, 16, v98
	v_lshlrev_b32_e32 v127, 16, v99
	v_and_b32_e32 v125, 0xffff0000, v99
	v_mov_b32_e32 v97, v129
	v_pk_add_f32 v[96:97], v[120:121], v[96:97]
	v_pk_add_f32 v[98:99], v[126:127], v[124:125]
	s_nop 0
	v_pk_add_f32 v[176:177], v[96:97], v[98:99]
	s_waitcnt vmcnt(1)
	v_mov_b64_e32 v[96:97], v[224:225]
	v_pk_add_f32 v[176:177], v[176:177], v[176:177] op_sel:[0,1] op_sel_hi:[1,0]
	v_lshlrev_b32_e32 v99, 16, v183
	v_lshlrev_b32_e32 v123, 16, v97
	v_lshlrev_b32_e32 v122, 16, v96
	v_and_b32_e32 v197, 0xffff0000, v97
	v_and_b32_e32 v196, 0xffff0000, v96
	s_waitcnt vmcnt(0)
	v_mov_b64_e32 v[96:97], v[226:227]
	global_load_dwordx4 v[224:227], v[14:15], off
	global_load_dwordx4 v[228:231], v[16:17], off
	global_load_dwordx4 v[232:235], v[14:15], off offset:1024
	global_load_dwordx4 v[236:239], v[16:17], off offset:1024
	global_load_dwordx4 v[244:247], v[14:15], off offset:2048
	global_load_dwordx4 v[248:251], v[16:17], off offset:2048
	global_load_dwordx4 v[252:255], v[14:15], off offset:3072
	v_pk_add_f32 v[180:181], v[122:123], v[196:197]
	v_lshlrev_b32_e32 v100, 16, v182
	v_and_b32_e32 v101, 0xffff0000, v182
	v_pk_add_f32 v[180:181], v[180:181], v[180:181] op_sel:[0,1] op_sel_hi:[1,0]
	v_mov_b32_e32 v177, v100
	v_mov_b32_e32 v181, v101
	v_pk_add_f32 v[176:177], v[176:177], v[180:181]
	v_mov_b32_e32 v182, v137
	v_lshlrev_b32_e32 v116, 16, v96
	v_and_b32_e32 v117, 0xffff0000, v96
	v_lshlrev_b32_e32 v118, 16, v97
	v_and_b32_e32 v119, 0xffff0000, v97
	v_add_f32_e32 v98, v116, v117
	v_add_f32_e32 v96, v118, v119
	v_and_b32_e32 v97, 0xffff0000, v183
	v_pk_add_f32 v[180:181], v[98:99], v[96:97]
	v_mov_b32_e32 v183, v139
	v_pk_add_f32 v[176:177], v[176:177], v[180:181]
	v_mov_b32_e32 v181, v143
	v_add_f32_e32 v42, v176, v177
	ds_bpermute_b32 v10, v167, v42
	v_pk_mul_f32 v[142:143], v[142:143], v[142:143]
	v_mov_b32_e32 v180, v141
	v_pk_fma_f32 v[140:141], v[140:141], v[140:141], v[142:143]
	v_mov_b32_e32 v143, v138
	s_waitcnt lgkmcnt(0)
	v_add_f32_e32 v10, v42, v10
	ds_bpermute_b32 v40, v169, v10
	v_pk_mul_f32 v[138:139], v[138:139], v[138:139]
	v_mov_b32_e32 v142, v136
	v_pk_fma_f32 v[136:137], v[136:137], v[136:137], v[138:139]
	v_mov_b32_e32 v176, v77
	s_waitcnt lgkmcnt(0)
	v_add_f32_e32 v10, v10, v40
	ds_bpermute_b32 v40, v213, v10
	v_mov_b32_e32 v177, v145
	v_mov_b32_e32 v77, v144
	v_pk_add_f32 v[136:137], v[140:141], v[136:137]
	v_pk_mul_f32 v[138:139], v[176:177], v[176:177]
	s_waitcnt lgkmcnt(0)
	v_add_f32_e32 v10, v10, v40
	ds_bpermute_b32 v40, v214, v10
	v_pk_mul_f32 v[140:141], v[76:77], v[76:77]
	v_pk_add_f32 v[136:137], v[136:137], v[136:137] op_sel_hi:[0,1]
	v_pk_mov_b32 v[144:145], v[140:141], v[138:139] op_sel:[1,0]
	v_mov_b32_e32 v141, v139
	s_waitcnt lgkmcnt(0)
	v_add_f32_e32 v10, v10, v40
	ds_bpermute_b32 v40, v215, v10
	v_pk_add_f32 v[138:139], v[144:145], v[140:141]
	v_mul_f32_e32 v136, v57, v57
	v_pk_add_f32 v[138:139], v[138:139], v[138:139] op_sel_hi:[0,1]
	v_mul_f32_e32 v138, v59, v59
	s_waitcnt lgkmcnt(0)
	v_add_f32_e32 v10, v10, v40
	ds_bpermute_b32 v40, v216, v10
	v_pk_add_f32 v[136:137], v[138:139], v[136:137]
	s_waitcnt lgkmcnt(0)
	v_add_f32_e32 v46, v10, v40
	v_mul_f32_e32 v10, v64, v64
	v_pk_fma_f32 v[140:141], v[64:65], v[64:65], v[10:11] op_sel_hi:[1,1,0]
	v_mul_f32_e32 v10, v66, v66
	v_pk_fma_f32 v[144:145], v[66:67], v[66:67], v[10:11] op_sel_hi:[1,1,0]
	v_mul_f32_e32 v140, v9, v9
	v_mul_f32_e32 v144, v61, v61
	v_pk_add_f32 v[140:141], v[140:141], v[144:145]
	v_mul_f32_e32 v10, v2, v2
	v_pk_add_f32 v[136:137], v[140:141], v[136:137]
	v_mov_b32_e32 v140, v7
	v_mov_b32_e32 v141, v147
	v_mov_b32_e32 v7, v146
	v_pk_mul_f32 v[138:139], v[140:141], v[140:141]
	v_pk_mul_f32 v[144:145], v[6:7], v[6:7]
	v_pk_add_f32 v[136:137], v[136:137], v[136:137] op_sel_hi:[0,1]
	v_pk_mov_b32 v[146:147], v[144:145], v[138:139] op_sel:[1,0]
	v_mov_b32_e32 v145, v139
	v_pk_add_f32 v[138:139], v[146:147], v[144:145]
	v_pk_fma_f32 v[144:145], v[2:3], v[2:3], v[10:11] op_sel_hi:[1,1,0]
	v_mul_f32_e32 v10, v4, v4
	v_pk_add_f32 v[138:139], v[138:139], v[138:139] op_sel_hi:[0,1]
	v_pk_fma_f32 v[146:147], v[4:5], v[4:5], v[10:11] op_sel_hi:[1,1,0]
	v_mul_f32_e32 v144, v44, v44
	v_mul_f32_e32 v146, v45, v45
	v_mul_f32_e32 v138, v43, v43
	v_mul_f32_e32 v136, v41, v41
	v_pk_add_f32 v[144:145], v[144:145], v[146:147]
	v_pk_add_f32 v[136:137], v[138:139], v[136:137]
	v_fmac_f32_e32 v188, 0xba000000, v46
	v_pk_add_f32 v[136:137], v[144:145], v[136:137]
	v_fmac_f32_e32 v178, 0xba000000, v46
	v_add_f32_e32 v10, v136, v137
	v_fmac_f32_e32 v192, 0xba000000, v46
	v_fmac_f32_e32 v190, 0xba000000, v46
	v_fmac_f32_e32 v189, 0xba000000, v46
	v_fmac_f32_e32 v179, 0xba000000, v46
	v_fmac_f32_e32 v193, 0xba000000, v46
	v_fmac_f32_e32 v191, 0xba000000, v46
	v_fmac_f32_e32 v194, 0xba000000, v46
	v_fmac_f32_e32 v134, 0xba000000, v46
	v_fmac_f32_e32 v195, 0xba000000, v46
	v_fmac_f32_e32 v135, 0xba000000, v46
	v_fmac_f32_e32 v131, 0xba000000, v46
	v_fmac_f32_e32 v130, 0xba000000, v46
	v_fmac_f32_e32 v133, 0xba000000, v46
	v_fmac_f32_e32 v132, 0xba000000, v46
	v_fmac_f32_e32 v125, 0xba000000, v46
	v_fmac_f32_e32 v127, 0xba000000, v46
	v_fmac_f32_e32 v129, 0xba000000, v46
	v_fmac_f32_e32 v121, 0xba000000, v46
	v_fmac_f32_e32 v196, 0xba000000, v46
	v_fmac_f32_e32 v122, 0xba000000, v46
	v_fmac_f32_e32 v197, 0xba000000, v46
	v_fmac_f32_e32 v123, 0xba000000, v46
	v_fmac_f32_e32 v117, 0xba000000, v46
	v_fmac_f32_e32 v116, 0xba000000, v46
	v_fmac_f32_e32 v119, 0xba000000, v46
	v_fmac_f32_e32 v118, 0xba000000, v46
	v_fmac_f32_e32 v97, 0xba000000, v46
	v_fmac_f32_e32 v99, 0xba000000, v46
	v_fmac_f32_e32 v101, 0xba000000, v46
	v_fmac_f32_e32 v100, 0xba000000, v46
	ds_bpermute_b32 v46, v167, v10
	v_pk_mul_f32 v[138:139], v[158:159], v[158:159]
	v_mov_b32_e32 v146, v157
	v_pk_fma_f32 v[144:145], v[156:157], v[156:157], v[138:139]
	v_mov_b32_e32 v157, v155
	s_waitcnt lgkmcnt(0)
; template <bool WB = true>
; __device__ __forceinline__ void ln1_phase(const bf16_t* buf, bf16_t* h1b, unsigned* xqs, float* sx, const float* gam, const float* bet, int G, int b) {
;     ...
;         for (int q = 0; q < R; ++q) { sq[q] = 0.f;
; #pragma unroll
;             for (int j = 0; j < 8; ++j) { v[q][j] = v[q][j] - sum[q]; sq[q] += (v[q][j].x * v[q][j].x + v[q][j].y * v[q][j].y) + (v[q][j].z * v[q][j].z + v[q][j].w * v[q][j].w); } }
; #pragma unroll
;         for (int q = 0; q < R; ++q) sq[q] = 1.0f / sqrtf(wave_sum(sq[q]) * (1.0f / D_) + LN_EPS);
	v_add_f32_e32 v10, v10, v46
	ds_bpermute_b32 v46, v169, v10
	v_mov_b32_e32 v139, v154
	v_pk_mul_f32 v[154:155], v[154:155], v[154:155]
	v_mov_b32_e32 v136, v156
	v_mov_b32_e32 v156, v153
	s_waitcnt lgkmcnt(0)
	v_add_f32_e32 v10, v10, v46
	ds_bpermute_b32 v46, v213, v10
	v_mov_b32_e32 v138, v152
	v_pk_fma_f32 v[152:153], v[152:153], v[152:153], v[154:155]
	v_mul_f32_e32 v40, v84, v84
	v_pk_add_f32 v[144:145], v[144:145], v[152:153]
	s_waitcnt lgkmcnt(0)
	v_add_f32_e32 v10, v10, v46
	ds_bpermute_b32 v46, v214, v10
	v_pk_mul_f32 v[152:153], v[186:187], v[186:187]
	v_pk_add_f32 v[144:145], v[144:145], v[144:145] op_sel_hi:[0,1]
	v_pk_mov_b32 v[154:155], v[150:151], v[152:153] op_sel:[1,0]
	v_mov_b32_e32 v151, v153
	s_waitcnt lgkmcnt(0)
	v_add_f32_e32 v10, v10, v46
	ds_bpermute_b32 v46, v215, v10
	v_pk_add_f32 v[150:151], v[154:155], v[150:151]
	v_pk_fma_f32 v[152:153], v[84:85], v[84:85], v[40:41] op_sel_hi:[1,1,0]
	v_mul_f32_e32 v40, v86, v86
	v_pk_add_f32 v[150:151], v[150:151], v[150:151] op_sel_hi:[0,1]
	s_waitcnt lgkmcnt(0)
	v_add_f32_e32 v10, v10, v46
	ds_bpermute_b32 v46, v216, v10
	v_pk_fma_f32 v[154:155], v[86:87], v[86:87], v[40:41] op_sel_hi:[1,1,0]
	v_mul_f32_e32 v152, v69, v69
	v_mul_f32_e32 v154, v75, v75
	v_mul_f32_e32 v150, v73, v73
	s_waitcnt lgkmcnt(0)
	v_add_f32_e32 v10, v10, v46
	v_fmamk_f32 v10, v10, 0x3a000000, v217
	v_cmp_gt_f32_e32 vcc, s45, v10
	v_mul_f32_e32 v46, 0x4f800000, v10
	v_mul_f32_e32 v144, v71, v71
	v_cndmask_b32_e32 v10, v10, v46, vcc
	v_sqrt_f32_e32 v46, v10
	v_pk_add_f32 v[152:153], v[152:153], v[154:155]
	v_pk_add_f32 v[144:145], v[150:151], v[144:145]
	v_mov_b32_e32 v150, v63
	v_add_u32_e32 v48, -1, v46
	v_fma_f32 v56, -v48, v46, v10
	v_cmp_ge_f32_e64 s[0:1], 0, v56
	v_add_u32_e32 v56, 1, v46
	v_mov_b32_e32 v151, v149
	v_cndmask_b32_e64 v48, v46, v48, s[0:1]
	v_fma_f32 v46, -v56, v46, v10
	v_cmp_lt_f32_e64 s[0:1], 0, v46
	v_mov_b32_e32 v63, v148
	v_pk_add_f32 v[144:145], v[152:153], v[144:145]
	v_cndmask_b32_e64 v46, v48, v56, s[0:1]
	v_mul_f32_e32 v48, 0x37800000, v46
	v_cndmask_b32_e32 v46, v46, v48, vcc
	v_cmp_class_f32_e32 vcc, v10, v218
	v_pk_mul_f32 v[152:153], v[150:151], v[150:151]
	v_pk_mul_f32 v[148:149], v[62:63], v[62:63]
	v_cndmask_b32_e32 v10, v46, v10, vcc
	v_div_scale_f32 v46, s[0:1], v10, v10, 1.0
	v_rcp_f32_e32 v48, v46
	v_pk_mov_b32 v[154:155], v[148:149], v[152:153] op_sel:[1,0]
	v_mov_b32_e32 v149, v153
	v_mul_f32_e32 v40, v52, v52
	v_fma_f32 v56, -v46, v48, 1.0
	v_pk_add_f32 v[148:149], v[154:155], v[148:149]
	v_pk_fma_f32 v[152:153], v[52:53], v[52:53], v[40:41] op_sel_hi:[1,1,0]
	v_mul_f32_e32 v40, v54, v54
	v_fmac_f32_e32 v48, v56, v48
	v_div_scale_f32 v56, vcc, 1.0, v10, 1.0
	v_pk_add_f32 v[144:145], v[144:145], v[144:145] op_sel_hi:[0,1]
	v_pk_add_f32 v[148:149], v[148:149], v[148:149] op_sel_hi:[0,1]
	v_pk_fma_f32 v[154:155], v[54:55], v[54:55], v[40:41] op_sel_hi:[1,1,0]
	v_mul_f32_e32 v58, v56, v48
	v_mul_f32_e32 v152, v50, v50
	v_mul_f32_e32 v154, v51, v51
	v_mul_f32_e32 v148, v49, v49
	v_mul_f32_e32 v144, v47, v47
	v_fma_f32 v60, -v46, v58, v56
	v_pk_add_f32 v[152:153], v[152:153], v[154:155]
	v_pk_add_f32 v[144:145], v[148:149], v[144:145]
	v_fmac_f32_e32 v58, v60, v48
	v_pk_add_f32 v[144:145], v[152:153], v[144:145]
	v_fma_f32 v46, -v46, v58, v56
	v_add_f32_e32 v42, v144, v145
	v_div_fmas_f32 v46, v46, v48, v58
	v_div_fixup_f32 v10, v46, v10, 1.0
	ds_bpermute_b32 v46, v167, v42
	v_pk_mul_f32 v[152:153], v[170:171], v[170:171]
	v_pk_mul_f32 v[154:155], v[162:163], v[162:163]
	v_mov_b32_e32 v147, v159
	v_mov_b32_e32 v148, v165
	s_waitcnt lgkmcnt(0)
	v_add_f32_e32 v42, v42, v46
	ds_bpermute_b32 v46, v169, v42
	v_pk_fma_f32 v[152:153], v[164:165], v[164:165], v[152:153]
	v_mov_b32_e32 v159, v163
	v_mov_b32_e32 v165, v162
	v_pk_fma_f32 v[154:155], v[160:161], v[160:161], v[154:155]
	s_waitcnt lgkmcnt(0)
	v_add_f32_e32 v42, v42, v46
	ds_bpermute_b32 v46, v213, v42
	v_mov_b32_e32 v162, v105
	v_mov_b32_e32 v163, v173
	v_mov_b32_e32 v105, v172
	v_mov_b32_e32 v137, v158
	s_waitcnt lgkmcnt(0)
	v_add_f32_e32 v42, v42, v46
	ds_bpermute_b32 v46, v214, v42
	v_mov_b32_e32 v144, v164
	v_mov_b32_e32 v158, v161
	v_mov_b32_e32 v164, v160
	v_pk_add_f32 v[152:153], v[152:153], v[154:155]
	s_waitcnt lgkmcnt(0)
	v_add_f32_e32 v42, v42, v46
	ds_bpermute_b32 v46, v215, v42
	v_pk_mul_f32 v[154:155], v[162:163], v[162:163]
	v_pk_mul_f32 v[160:161], v[104:105], v[104:105]
	v_mov_b32_e32 v149, v171
	v_mov_b32_e32 v145, v170
	s_waitcnt lgkmcnt(0)
	v_add_f32_e32 v42, v42, v46
	ds_bpermute_b32 v46, v216, v42
	v_pk_mov_b32 v[170:171], v[160:161], v[154:155] op_sel:[1,0]
	v_mov_b32_e32 v161, v155
	v_mul_f32_e32 v40, v112, v112
	v_pk_add_f32 v[154:155], v[170:171], v[160:161]
	s_waitcnt lgkmcnt(0)
; template <bool WB = true>
; __device__ __forceinline__ void ln1_phase(const bf16_t* buf, bf16_t* h1b, unsigned* xqs, float* sx, const float* gam, const float* bet, int G, int b) {
;     ...
;         for (int q = 0; q < R; ++q) { sq[q] = 0.f;
; #pragma unroll
;             for (int j = 0; j < 8; ++j) { v[q][j] = v[q][j] - sum[q]; sq[q] += (v[q][j].x * v[q][j].x + v[q][j].y * v[q][j].y) + (v[q][j].z * v[q][j].z + v[q][j].w * v[q][j].w); } }
; #pragma unroll
;         for (int q = 0; q < R; ++q) sq[q] = 1.0f / sqrtf(wave_sum(sq[q]) * (1.0f / D_) + LN_EPS);
; #pragma unroll
;         for (int j = 0; j < 8; ++j) {
;             const f32x4 gg = *(const f32x4*)(gam + 256 * j + 4 * lane), bb = *(const f32x4*)(bet + 256 * j + 4 * lane);
; #pragma unroll
;             for (int q = 0; q < R; ++q) v[q][j] = v[q][j] * sq[q] * gg + bb;
	v_add_f32_e32 v42, v42, v46
	v_fmamk_f32 v42, v42, 0x3a000000, v217
	v_cmp_gt_f32_e32 vcc, s45, v42
	v_mul_f32_e32 v46, 0x4f800000, v42
	v_pk_fma_f32 v[160:161], v[112:113], v[112:113], v[40:41] op_sel_hi:[1,1,0]
	v_cndmask_b32_e32 v42, v42, v46, vcc
	v_sqrt_f32_e32 v46, v42
	v_mul_f32_e32 v40, v114, v114
	v_pk_add_f32 v[152:153], v[152:153], v[152:153] op_sel_hi:[0,1]
	v_pk_add_f32 v[154:155], v[154:155], v[154:155] op_sel_hi:[0,1]
	v_add_u32_e32 v48, -1, v46
	v_fma_f32 v56, -v48, v46, v42
	v_cmp_ge_f32_e64 s[0:1], 0, v56
	v_add_u32_e32 v56, 1, v46
	v_pk_fma_f32 v[170:171], v[114:115], v[114:115], v[40:41] op_sel_hi:[1,1,0]
	v_cndmask_b32_e64 v48, v46, v48, s[0:1]
	v_fma_f32 v46, -v56, v46, v42
	v_cmp_lt_f32_e64 s[0:1], 0, v46
	v_mul_f32_e32 v160, v91, v91
	v_mul_f32_e32 v170, v111, v111
	v_cndmask_b32_e64 v46, v48, v56, s[0:1]
	v_mul_f32_e32 v48, 0x37800000, v46
	v_cndmask_b32_e32 v46, v46, v48, vcc
	v_cmp_class_f32_e32 vcc, v42, v218
	v_mul_f32_e32 v154, v109, v109
	v_mul_f32_e32 v152, v107, v107
	v_cndmask_b32_e32 v42, v46, v42, vcc
	v_div_scale_f32 v46, s[0:1], v42, v42, 1.0
	v_rcp_f32_e32 v48, v46
	v_pk_add_f32 v[160:161], v[160:161], v[170:171]
	v_pk_add_f32 v[152:153], v[154:155], v[152:153]
	v_mul_f32_e32 v40, v92, v92
	v_pk_add_f32 v[152:153], v[160:161], v[152:153]
	v_mov_b32_e32 v160, v103
	v_mov_b32_e32 v161, v175
	v_mov_b32_e32 v103, v174
	v_pk_mul_f32 v[154:155], v[160:161], v[160:161]
	v_pk_mul_f32 v[170:171], v[102:103], v[102:103]
	v_fma_f32 v56, -v46, v48, 1.0
	v_pk_mov_b32 v[172:173], v[170:171], v[154:155] op_sel:[1,0]
	v_mov_b32_e32 v171, v155
	v_pk_add_f32 v[154:155], v[172:173], v[170:171]
	v_pk_fma_f32 v[170:171], v[92:93], v[92:93], v[40:41] op_sel_hi:[1,1,0]
	v_mul_f32_e32 v40, v94, v94
	v_fmac_f32_e32 v48, v56, v48
	v_div_scale_f32 v56, vcc, 1.0, v42, 1.0
	v_pk_add_f32 v[152:153], v[152:153], v[152:153] op_sel_hi:[0,1]
	v_pk_add_f32 v[154:155], v[154:155], v[154:155] op_sel_hi:[0,1]
	v_pk_fma_f32 v[172:173], v[94:95], v[94:95], v[40:41] op_sel_hi:[1,1,0]
	v_mul_f32_e32 v58, v56, v48
	v_mul_f32_e32 v170, v82, v82
	v_mul_f32_e32 v172, v83, v83
	v_mul_f32_e32 v154, v81, v81
	v_mul_f32_e32 v152, v79, v79
	v_fma_f32 v60, -v46, v58, v56
	v_pk_add_f32 v[170:171], v[170:171], v[172:173]
	v_pk_add_f32 v[152:153], v[154:155], v[152:153]
	v_fmac_f32_e32 v58, v60, v48
	v_pk_add_f32 v[152:153], v[170:171], v[152:153]
	v_fma_f32 v46, -v46, v58, v56
	v_add_f32_e32 v40, v152, v153
	v_div_fmas_f32 v46, v46, v48, v58
	v_div_fixup_f32 v42, v46, v42, 1.0
	ds_bpermute_b32 v46, v167, v40
	v_pk_mul_f32 v[152:153], v[192:193], v[192:193]
	v_pk_mul_f32 v[154:155], v[188:189], v[188:189]
	v_mov_b32_e32 v199, v193
	v_mov_b32_e32 v170, v190
	s_waitcnt lgkmcnt(0)
	v_add_f32_e32 v40, v40, v46
	ds_bpermute_b32 v46, v169, v40
	v_mov_b32_e32 v171, v192
	v_pk_fma_f32 v[152:153], v[190:191], v[190:191], v[152:153]
	v_mov_b32_e32 v190, v179
	v_mov_b32_e32 v200, v178
	s_waitcnt lgkmcnt(0)
	v_add_f32_e32 v40, v40, v46
	ds_bpermute_b32 v46, v213, v40
	v_pk_fma_f32 v[154:155], v[178:179], v[178:179], v[154:155]
	v_mov_b32_e32 v192, v135
	v_mov_b32_e32 v193, v195
	v_mov_b32_e32 v135, v194
	s_waitcnt lgkmcnt(0)
	v_add_f32_e32 v40, v40, v46
	ds_bpermute_b32 v46, v214, v40
	v_mov_b32_e32 v178, v123
	v_mov_b32_e32 v179, v197
	v_mov_b32_e32 v123, v196
	s_waitcnt vmcnt(6)
	v_mov_b64_e32 v[194:195], v[224:225]
	v_mov_b64_e32 v[196:197], v[226:227]
	global_load_dwordx4 v[224:227], v[16:17], off offset:3072
	s_waitcnt vmcnt(6)
	v_mov_b64_e32 v[220:221], v[228:229]
	v_mov_b64_e32 v[222:223], v[230:231]
	global_load_dwordx4 v[228:231], v[20:21], off
	s_waitcnt lgkmcnt(0)
	v_add_f32_e32 v40, v40, v46
	ds_bpermute_b32 v46, v215, v40
	v_pk_add_f32 v[152:153], v[152:153], v[154:155]
	v_pk_mul_f32 v[154:155], v[192:193], v[192:193]
	v_pk_mul_f32 v[172:173], v[134:135], v[134:135]
	v_mul_f32_e32 v8, v130, v130
	s_waitcnt lgkmcnt(0)
	v_add_f32_e32 v40, v40, v46
	ds_bpermute_b32 v46, v216, v40
	v_pk_mov_b32 v[174:175], v[172:173], v[154:155] op_sel:[1,0]
	v_mov_b32_e32 v173, v155
	v_pk_add_f32 v[154:155], v[174:175], v[172:173]
	v_pk_fma_f32 v[172:173], v[130:131], v[130:131], v[8:9] op_sel_hi:[1,1,0]
	s_waitcnt lgkmcnt(0)
	v_add_f32_e32 v40, v40, v46
	v_fmamk_f32 v40, v40, 0x3a000000, v217
	v_cmp_gt_f32_e32 vcc, s45, v40
	v_mul_f32_e32 v46, 0x4f800000, v40
	v_mul_f32_e32 v8, v132, v132
	v_cndmask_b32_e32 v40, v40, v46, vcc
	v_sqrt_f32_e32 v46, v40
	v_pk_add_f32 v[152:153], v[152:153], v[152:153] op_sel_hi:[0,1]
	v_pk_add_f32 v[154:155], v[154:155], v[154:155] op_sel_hi:[0,1]
	v_pk_fma_f32 v[174:175], v[132:133], v[132:133], v[8:9] op_sel_hi:[1,1,0]
	v_add_u32_e32 v48, -1, v46
	v_fma_f32 v56, -v48, v46, v40
	v_cmp_ge_f32_e64 s[0:1], 0, v56
	v_add_u32_e32 v56, 1, v46
	v_mul_f32_e32 v172, v121, v121
	v_cndmask_b32_e64 v48, v46, v48, s[0:1]
	v_fma_f32 v46, -v56, v46, v40
	v_cmp_lt_f32_e64 s[0:1], 0, v46
	v_mul_f32_e32 v174, v129, v129
	v_mul_f32_e32 v154, v127, v127
	v_cndmask_b32_e64 v46, v48, v56, s[0:1]
	v_mul_f32_e32 v48, 0x37800000, v46
	v_cndmask_b32_e32 v46, v46, v48, vcc
	v_cmp_class_f32_e32 vcc, v40, v218
	v_mul_f32_e32 v152, v125, v125
	v_pk_add_f32 v[172:173], v[172:173], v[174:175]
	v_cndmask_b32_e32 v40, v46, v40, vcc
	v_div_scale_f32 v46, s[0:1], v40, v40, 1.0
	v_rcp_f32_e32 v48, v46
	v_pk_add_f32 v[152:153], v[154:155], v[152:153]
	v_pk_mul_f32 v[154:155], v[178:179], v[178:179]
	v_pk_add_f32 v[152:153], v[172:173], v[152:153]
	v_pk_mul_f32 v[172:173], v[122:123], v[122:123]
	v_mul_f32_e32 v8, v116, v116
	v_pk_mov_b32 v[174:175], v[172:173], v[154:155] op_sel:[1,0]
	v_mov_b32_e32 v173, v155
	v_fma_f32 v56, -v46, v48, 1.0
	v_pk_add_f32 v[154:155], v[174:175], v[172:173]
	v_pk_fma_f32 v[172:173], v[116:117], v[116:117], v[8:9] op_sel_hi:[1,1,0]
	v_mul_f32_e32 v8, v118, v118
	v_fmac_f32_e32 v48, v56, v48
	v_div_scale_f32 v56, vcc, 1.0, v40, 1.0
	v_pk_add_f32 v[152:153], v[152:153], v[152:153] op_sel_hi:[0,1]
	v_pk_add_f32 v[154:155], v[154:155], v[154:155] op_sel_hi:[0,1]
	v_pk_fma_f32 v[174:175], v[118:119], v[118:119], v[8:9] op_sel_hi:[1,1,0]
	v_mul_f32_e32 v58, v56, v48
	v_mul_f32_e32 v172, v100, v100
	v_mul_f32_e32 v174, v101, v101
	v_mul_f32_e32 v154, v99, v99
	v_mul_f32_e32 v152, v97, v97
	v_fma_f32 v60, -v46, v58, v56
	v_pk_add_f32 v[172:173], v[172:173], v[174:175]
	v_pk_add_f32 v[152:153], v[154:155], v[152:153]
	v_fmac_f32_e32 v58, v60, v48
	v_pk_add_f32 v[152:153], v[172:173], v[152:153]
	v_fma_f32 v46, -v46, v58, v56
	v_add_f32_e32 v8, v152, v153
	v_div_fmas_f32 v46, v46, v48, v58
	v_div_fixup_f32 v48, v46, v40, 1.0
	ds_bpermute_b32 v40, v167, v8
	v_pk_mul_f32 v[152:153], v[184:185], v[10:11] op_sel_hi:[1,0]
	v_pk_mul_f32 v[136:137], v[136:137], v[42:43] op_sel_hi:[1,0]
	v_pk_mul_f32 v[138:139], v[138:139], v[42:43] op_sel_hi:[1,0]
	v_mov_b32_e32 v201, v188
	s_waitcnt lgkmcnt(0)
; template <bool WB = true>
; __device__ __forceinline__ void ln1_phase(const bf16_t* buf, bf16_t* h1b, unsigned* xqs, float* sx, const float* gam, const float* bet, int G, int b) {
;     ...
;         for (int q = 0; q < R; ++q) sq[q] = 1.0f / sqrtf(wave_sum(sq[q]) * (1.0f / D_) + LN_EPS);
; #pragma unroll
;         for (int j = 0; j < 8; ++j) {
;             const f32x4 gg = *(const f32x4*)(gam + 256 * j + 4 * lane), bb = *(const f32x4*)(bet + 256 * j + 4 * lane);
; #pragma unroll
;             for (int q = 0; q < R; ++q) v[q][j] = v[q][j] * sq[q] * gg + bb;
	v_add_f32_e32 v8, v8, v40
	ds_bpermute_b32 v40, v169, v8
	v_pk_mul_f32 v[142:143], v[142:143], v[10:11] op_sel_hi:[1,0]
	v_pk_fma_f32 v[174:175], v[152:153], v[194:195], v[220:221]
	v_pk_fma_f32 v[152:153], v[138:139], v[196:197], v[222:223]
	v_pk_fma_f32 v[154:155], v[136:137], v[194:195], v[220:221]
	s_waitcnt lgkmcnt(0)
	v_add_f32_e32 v8, v8, v40
	ds_bpermute_b32 v40, v213, v8
	v_pk_mul_f32 v[136:137], v[144:145], v[48:49] op_sel_hi:[1,0]
	v_pk_mul_f32 v[138:139], v[164:165], v[48:49] op_sel_hi:[1,0]
	v_pk_fma_f32 v[172:173], v[142:143], v[196:197], v[222:223]
	v_pk_fma_f32 v[142:143], v[196:197], v[138:139], v[222:223]
	s_waitcnt lgkmcnt(0)
	v_add_f32_e32 v8, v8, v40
	ds_bpermute_b32 v40, v214, v8
	v_pk_fma_f32 v[144:145], v[194:195], v[136:137], v[220:221]
	v_pk_mul_f32 v[146:147], v[146:147], v[42:43] op_sel_hi:[1,0]
	v_mov_b32_e32 v198, v191
	v_mov_b32_e32 v191, v189
	s_waitcnt lgkmcnt(0)
	v_add_f32_e32 v8, v8, v40
	ds_bpermute_b32 v40, v215, v8
	v_pk_mul_f32 v[164:165], v[180:181], v[10:11] op_sel_hi:[1,0]
	v_pk_mul_f32 v[156:157], v[156:157], v[42:43] op_sel_hi:[1,0]
	v_pk_mul_f32 v[76:77], v[76:77], v[10:11] op_sel_hi:[1,0]
	v_pk_mul_f32 v[176:177], v[176:177], v[10:11] op_sel_hi:[1,0]
	s_waitcnt lgkmcnt(0)
	v_add_f32_e32 v8, v8, v40
	ds_bpermute_b32 v40, v216, v8
	v_pk_mul_f32 v[64:65], v[64:65], v[10:11] op_sel_hi:[1,0]
	v_pk_mul_f32 v[66:67], v[66:67], v[10:11] op_sel_hi:[1,0]
	v_mov_b32_e32 v128, v121
	v_mov_b32_e32 v124, v127
	s_waitcnt lgkmcnt(0)
	v_add_f32_e32 v8, v8, v40
	v_fmamk_f32 v8, v8, 0x3a000000, v217
	v_cmp_gt_f32_e32 vcc, s45, v8
	v_mul_f32_e32 v40, 0x4f800000, v8
	v_pk_mul_f32 v[6:7], v[6:7], v[10:11] op_sel_hi:[1,0]
	v_cndmask_b32_e32 v8, v8, v40, vcc
	v_sqrt_f32_e32 v40, v8
	v_pk_mul_f32 v[2:3], v[2:3], v[10:11] op_sel_hi:[1,0]
	v_pk_mul_f32 v[4:5], v[4:5], v[10:11] op_sel_hi:[1,0]
	v_pk_mul_f32 v[44:45], v[44:45], v[10:11] op_sel_hi:[1,0]
	v_add_u32_e32 v46, -1, v40
	v_fma_f32 v56, -v46, v40, v8
	v_cmp_ge_f32_e64 s[0:1], 0, v56
	v_add_u32_e32 v56, 1, v40
	v_mov_b32_e32 v96, v99
	v_cndmask_b32_e64 v46, v40, v46, s[0:1]
	v_fma_f32 v40, -v56, v40, v8
	v_cmp_lt_f32_e64 s[0:1], 0, v40
	s_nop 1
	v_cndmask_b32_e64 v40, v46, v56, s[0:1]
	v_mul_f32_e32 v46, 0x37800000, v40
	v_cndmask_b32_e32 v40, v40, v46, vcc
	v_cmp_class_f32_e32 vcc, v8, v218
	s_nop 1
	v_cndmask_b32_e32 v8, v40, v8, vcc
	v_div_scale_f32 v40, s[0:1], v8, v8, 1.0
	v_rcp_f32_e32 v46, v40
	s_nop 0
	v_fma_f32 v56, -v40, v46, 1.0
	v_fmac_f32_e32 v46, v56, v46
	v_div_scale_f32 v56, vcc, 1.0, v8, 1.0
	v_mul_f32_e32 v58, v56, v46
	v_fma_f32 v60, -v40, v58, v56
	v_fmac_f32_e32 v58, v60, v46
	v_fma_f32 v40, -v40, v58, v56
	v_div_fmas_f32 v40, v40, v46, v58
	v_div_fixup_f32 v72, v40, v8, 1.0
	v_pk_mul_f32 v[138:139], v[170:171], v[72:73] op_sel_hi:[1,0]
	v_pk_mul_f32 v[136:137], v[200:201], v[72:73] op_sel_hi:[1,0]
	v_pk_fma_f32 v[138:139], v[194:195], v[138:139], v[220:221]
	v_pk_fma_f32 v[136:137], v[196:197], v[136:137], v[222:223]
	s_waitcnt vmcnt(6)
	v_mov_b64_e32 v[194:195], v[232:233]
	v_mov_b64_e32 v[196:197], v[234:235]
	global_load_dwordx4 v[232:235], v[22:23], off
	s_waitcnt vmcnt(6)
	v_mov_b64_e32 v[220:221], v[236:237]
	v_mov_b64_e32 v[222:223], v[238:239]
	global_load_dwordx4 v[236:239], v[24:25], off
	v_pk_mul_f32 v[170:171], v[182:183], v[10:11] op_sel_hi:[1,0]
	v_mov_b32_e32 v60, v9
	v_mov_b32_e32 v56, v59
	v_pk_mul_f32 v[8:9], v[60:61], v[10:11] op_sel_hi:[1,0]
	v_pk_mul_f32 v[56:57], v[56:57], v[10:11] op_sel_hi:[1,0]
	v_mov_b32_e32 v40, v43
	v_pk_mul_f32 v[40:41], v[40:41], v[10:11] op_sel_hi:[1,0]
	v_mov_b32_e32 v46, v49
	v_pk_fma_f32 v[182:183], v[170:171], v[196:197], v[222:223]
	v_pk_fma_f32 v[170:171], v[146:147], v[194:195], v[220:221]
	v_pk_mul_f32 v[146:147], v[148:149], v[48:49] op_sel_hi:[1,0]
	v_pk_mul_f32 v[148:149], v[158:159], v[48:49] op_sel_hi:[1,0]
	v_pk_fma_f32 v[184:185], v[164:165], v[194:195], v[220:221]
	v_pk_fma_f32 v[164:165], v[156:157], v[196:197], v[222:223]
	v_pk_fma_f32 v[156:157], v[196:197], v[148:149], v[222:223]
	v_pk_fma_f32 v[158:159], v[194:195], v[146:147], v[220:221]
	v_pk_mul_f32 v[148:149], v[198:199], v[72:73] op_sel_hi:[1,0]
	v_pk_mul_f32 v[146:147], v[190:191], v[72:73] op_sel_hi:[1,0]
	v_pk_fma_f32 v[148:149], v[194:195], v[148:149], v[220:221]
	v_pk_fma_f32 v[146:147], v[196:197], v[146:147], v[222:223]
	s_waitcnt vmcnt(6)
	v_mov_b64_e32 v[194:195], v[244:245]
	v_mov_b64_e32 v[196:197], v[246:247]
	global_load_dwordx4 v[244:247], v[26:27], off
	s_waitcnt vmcnt(6)
	v_mov_b64_e32 v[198:199], v[248:249]
	v_mov_b64_e32 v[200:201], v[250:251]
	global_load_dwordx4 v[248:251], v[28:29], off
	v_pk_fma_f32 v[190:191], v[76:77], v[194:195], v[198:199]
	v_pk_mul_f32 v[76:77], v[88:89], v[42:43] op_sel_hi:[1,0]
	v_pk_mul_f32 v[88:89], v[186:187], v[42:43] op_sel_hi:[1,0]
	v_pk_fma_f32 v[188:189], v[176:177], v[196:197], v[200:201]
	v_pk_fma_f32 v[176:177], v[88:89], v[196:197], v[200:201]
	v_pk_fma_f32 v[180:181], v[76:77], v[194:195], v[198:199]
	v_pk_mul_f32 v[76:77], v[104:105], v[48:49] op_sel_hi:[1,0]
	v_pk_mul_f32 v[88:89], v[162:163], v[48:49] op_sel_hi:[1,0]
	v_pk_fma_f32 v[162:163], v[76:77], v[194:195], v[198:199]
	v_pk_fma_f32 v[104:105], v[88:89], v[196:197], v[200:201]
	v_pk_mul_f32 v[88:89], v[134:135], v[72:73] op_sel_hi:[1,0]
	v_pk_mul_f32 v[76:77], v[192:193], v[72:73] op_sel_hi:[1,0]
	v_pk_fma_f32 v[88:89], v[194:195], v[88:89], v[198:199]
	v_pk_fma_f32 v[76:77], v[196:197], v[76:77], v[200:201]
	s_waitcnt vmcnt(6)
	v_mov_b64_e32 v[196:197], v[252:253]
	v_mov_b64_e32 v[198:199], v[254:255]
	global_load_dwordx4 v[252:255], v[30:31], off
	s_waitcnt vmcnt(6)
; template <bool WB = true>
; __device__ __forceinline__ void ln1_phase(const bf16_t* buf, bf16_t* h1b, unsigned* xqs, float* sx, const float* gam, const float* bet, int G, int b) {
;     ...
;         for (int j = 0; j < 8; ++j) {
;             const f32x4 gg = *(const f32x4*)(gam + 256 * j + 4 * lane), bb = *(const f32x4*)(bet + 256 * j + 4 * lane);
; #pragma unroll
;             for (int q = 0; q < R; ++q) v[q][j] = v[q][j] * sq[q] * gg + bb;
;         }
; #pragma unroll
;         for (int q = 0; q < R; ++q) { amax[q] = 0.f;
; #pragma unroll
;             for (int j = 0; j < 8; ++j) amax[q] = fmaxf(amax[q], fmaxf(fmaxf(fabsf(v[q][j].x), fabsf(v[q][j].y)), fmaxf(fabsf(v[q][j].z), fabsf(v[q][j].w)))); }
	v_mov_b64_e32 v[220:221], v[224:225]
	v_mov_b64_e32 v[222:223], v[226:227]
	global_load_dwordx4 v[224:227], v[32:33], off
	v_pk_fma_f32 v[192:193], v[66:67], v[198:199], v[222:223]
	v_pk_fma_f32 v[194:195], v[64:65], v[196:197], v[220:221]
	v_pk_mul_f32 v[64:65], v[84:85], v[42:43] op_sel_hi:[1,0]
	v_pk_mul_f32 v[66:67], v[86:87], v[42:43] op_sel_hi:[1,0]
	v_pk_fma_f32 v[186:187], v[64:65], v[196:197], v[220:221]
	v_pk_fma_f32 v[134:135], v[66:67], v[198:199], v[222:223]
	v_pk_mul_f32 v[64:65], v[112:113], v[48:49] op_sel_hi:[1,0]
	v_pk_mul_f32 v[66:67], v[114:115], v[48:49] op_sel_hi:[1,0]
	v_pk_fma_f32 v[86:87], v[64:65], v[196:197], v[220:221]
	v_pk_fma_f32 v[84:85], v[66:67], v[198:199], v[222:223]
	v_pk_mul_f32 v[66:67], v[130:131], v[72:73] op_sel_hi:[1,0]
	v_pk_mul_f32 v[64:65], v[132:133], v[72:73] op_sel_hi:[1,0]
	v_pk_fma_f32 v[66:67], v[196:197], v[66:67], v[220:221]
	v_pk_fma_f32 v[64:65], v[198:199], v[64:65], v[222:223]
	s_waitcnt vmcnt(6)
	v_mov_b64_e32 v[196:197], v[228:229]
	v_mov_b64_e32 v[198:199], v[230:231]
	global_load_dwordx4 v[228:231], v[34:35], off
	s_waitcnt vmcnt(6)
	v_mov_b64_e32 v[220:221], v[232:233]
	v_mov_b64_e32 v[222:223], v[234:235]
	v_pk_fma_f32 v[114:115], v[56:57], v[198:199], v[222:223]
	v_pk_fma_f32 v[130:131], v[8:9], v[196:197], v[220:221]
	v_pk_mul_f32 v[8:9], v[74:75], v[42:43] op_sel_hi:[1,0]
	v_pk_mul_f32 v[56:57], v[70:71], v[42:43] op_sel_hi:[1,0]
	v_pk_fma_f32 v[112:113], v[8:9], v[196:197], v[220:221]
	v_pk_fma_f32 v[74:75], v[56:57], v[198:199], v[222:223]
	v_pk_mul_f32 v[8:9], v[110:111], v[48:49] op_sel_hi:[1,0]
	v_pk_mul_f32 v[56:57], v[106:107], v[48:49] op_sel_hi:[1,0]
	v_pk_fma_f32 v[68:69], v[8:9], v[196:197], v[220:221]
	v_pk_fma_f32 v[60:61], v[56:57], v[198:199], v[222:223]
	v_pk_mul_f32 v[8:9], v[128:129], v[72:73] op_sel_hi:[1,0]
	v_pk_mul_f32 v[56:57], v[124:125], v[72:73] op_sel_hi:[1,0]
	v_pk_fma_f32 v[58:59], v[196:197], v[8:9], v[220:221]
	v_pk_fma_f32 v[56:57], v[198:199], v[56:57], v[222:223]
	s_waitcnt vmcnt(5)
	v_mov_b64_e32 v[196:197], v[236:237]
	v_mov_b64_e32 v[198:199], v[238:239]
	s_waitcnt vmcnt(4)
	v_mov_b64_e32 v[220:221], v[244:245]
	v_mov_b64_e32 v[222:223], v[246:247]
	v_pk_mul_f32 v[8:9], v[140:141], v[10:11] op_sel_hi:[1,0]
	v_max_f32_e64 v10, |v84|, |v85|
	v_max3_f32 v10, |v86|, |v87|, v10
	v_pk_fma_f32 v[124:125], v[8:9], v[198:199], v[222:223]
	v_pk_fma_f32 v[126:127], v[6:7], v[196:197], v[220:221]
	v_pk_mul_f32 v[6:7], v[62:63], v[42:43] op_sel_hi:[1,0]
	v_pk_mul_f32 v[8:9], v[150:151], v[42:43] op_sel_hi:[1,0]
	v_pk_fma_f32 v[108:109], v[6:7], v[196:197], v[220:221]
	v_pk_fma_f32 v[106:107], v[8:9], v[198:199], v[222:223]
	v_pk_mul_f32 v[6:7], v[102:103], v[48:49] op_sel_hi:[1,0]
	v_pk_mul_f32 v[8:9], v[160:161], v[48:49] op_sel_hi:[1,0]
	v_pk_fma_f32 v[102:103], v[6:7], v[196:197], v[220:221]
	v_pk_fma_f32 v[90:91], v[8:9], v[198:199], v[222:223]
	v_pk_mul_f32 v[6:7], v[122:123], v[72:73] op_sel_hi:[1,0]
	v_pk_mul_f32 v[8:9], v[178:179], v[72:73] op_sel_hi:[1,0]
	v_pk_fma_f32 v[70:71], v[6:7], v[196:197], v[220:221]
	v_pk_fma_f32 v[62:63], v[8:9], v[198:199], v[222:223]
	s_waitcnt vmcnt(3)
	v_mov_b64_e32 v[6:7], v[248:249]
	v_mov_b64_e32 v[8:9], v[250:251]
	s_waitcnt vmcnt(2)
	v_mov_b64_e32 v[196:197], v[252:253]
	v_mov_b64_e32 v[198:199], v[254:255]
	v_pk_fma_f32 v[122:123], v[4:5], v[8:9], v[198:199]
	v_pk_fma_f32 v[128:129], v[2:3], v[6:7], v[196:197]
	v_pk_mul_f32 v[2:3], v[52:53], v[42:43] op_sel_hi:[1,0]
	v_pk_mul_f32 v[4:5], v[54:55], v[42:43] op_sel_hi:[1,0]
	v_pk_fma_f32 v[120:121], v[2:3], v[6:7], v[196:197]
	v_pk_fma_f32 v[110:111], v[4:5], v[8:9], v[198:199]
	v_pk_mul_f32 v[2:3], v[92:93], v[48:49] op_sel_hi:[1,0]
	v_pk_mul_f32 v[4:5], v[94:95], v[48:49] op_sel_hi:[1,0]
	v_pk_fma_f32 v[94:95], v[2:3], v[6:7], v[196:197]
	v_pk_fma_f32 v[92:93], v[4:5], v[8:9], v[198:199]
	v_pk_mul_f32 v[2:3], v[116:117], v[72:73] op_sel_hi:[1,0]
	v_pk_mul_f32 v[4:5], v[118:119], v[72:73] op_sel_hi:[1,0]
	v_pk_fma_f32 v[54:55], v[2:3], v[6:7], v[196:197]
	v_pk_fma_f32 v[52:53], v[4:5], v[8:9], v[198:199]
	s_waitcnt vmcnt(1)
	v_mov_b64_e32 v[2:3], v[224:225]
	v_mov_b64_e32 v[4:5], v[226:227]
	s_waitcnt vmcnt(0)
; template <bool WB = true>
; __device__ __forceinline__ void ln1_phase(const bf16_t* buf, bf16_t* h1b, unsigned* xqs, float* sx, const float* gam, const float* bet, int G, int b) {
;     ...
;             for (int q = 0; q < R; ++q) v[q][j] = v[q][j] * sq[q] * gg + bb;
;         }
; #pragma unroll
;         for (int q = 0; q < R; ++q) { amax[q] = 0.f;
; #pragma unroll
;             for (int j = 0; j < 8; ++j) amax[q] = fmaxf(amax[q], fmaxf(fmaxf(fabsf(v[q][j].x), fabsf(v[q][j].y)), fmaxf(fabsf(v[q][j].z), fabsf(v[q][j].w)))); }
; #pragma unroll
;         for (int q = 0; q < R; ++q) amax[q] = wave_max(amax[q]);
; #pragma unroll
;         for (int q = 0; q < R; ++q) {
;             const int row = row0 + q * NGW;
;             if (row < S_) {
;                 const float inv = amax[q] > 0.f ? 127.0f / amax[q] : 0.f;
;                 if (lane == 0) sx[row] = amax[q] * (1.0f / 127.0f);
	v_mov_b64_e32 v[6:7], v[228:229]
	v_mov_b64_e32 v[8:9], v[230:231]
	v_pk_fma_f32 v[116:117], v[40:41], v[4:5], v[8:9]
	v_pk_mul_f32 v[40:41], v[50:51], v[42:43] op_sel_hi:[1,0]
	v_pk_mul_f32 v[42:43], v[46:47], v[42:43] op_sel_hi:[1,0]
	v_pk_fma_f32 v[118:119], v[44:45], v[2:3], v[6:7]
	v_pk_fma_f32 v[44:45], v[42:43], v[4:5], v[8:9]
	v_pk_fma_f32 v[46:47], v[40:41], v[2:3], v[6:7]
	v_pk_mul_f32 v[42:43], v[82:83], v[48:49] op_sel_hi:[1,0]
	v_pk_mul_f32 v[40:41], v[78:79], v[48:49] op_sel_hi:[1,0]
	v_pk_mul_f32 v[48:49], v[100:101], v[72:73] op_sel_hi:[1,0]
	v_pk_fma_f32 v[42:43], v[42:43], v[2:3], v[6:7]
	v_pk_fma_f32 v[2:3], v[48:49], v[2:3], v[6:7]
	v_max_f32_e64 v6, |v172|, |v173|
	v_max_f32_e64 v7, |v182|, |v183|
	v_pk_mul_f32 v[50:51], v[96:97], v[72:73] op_sel_hi:[1,0]
	v_max3_f32 v6, |v174|, |v175|, v6
	v_max3_f32 v7, |v184|, |v185|, v7
	v_pk_fma_f32 v[40:41], v[40:41], v[4:5], v[8:9]
	v_pk_fma_f32 v[4:5], v[50:51], v[4:5], v[8:9]
	v_max3_f32 v6, v6, 0, v7
	v_max_f32_e64 v7, |v188|, |v189|
	v_max_f32_e64 v8, |v192|, |v193|
	v_max3_f32 v7, |v190|, |v191|, v7
	v_max3_f32 v8, |v194|, |v195|, v8
	v_max3_f32 v6, v6, v7, v8
	v_max_f32_e64 v7, |v114|, |v115|
	v_max_f32_e64 v8, |v124|, |v125|
	v_max3_f32 v7, |v130|, |v131|, v7
	v_max3_f32 v8, |v126|, |v127|, v8
	v_max3_f32 v6, v6, v7, v8
	v_max_f32_e64 v7, |v122|, |v123|
	v_max_f32_e64 v8, |v116|, |v117|
	v_max3_f32 v7, |v128|, |v129|, v7
	v_max3_f32 v8, |v118|, |v119|, v8
	v_max3_f32 v6, v6, v7, v8
	v_max_f32_e64 v7, |v152|, |v153|
	v_max_f32_e64 v8, |v164|, |v165|
	v_max3_f32 v7, |v154|, |v155|, v7
	v_max3_f32 v8, |v170|, |v171|, v8
	v_max3_f32 v7, v7, 0, v8
	v_max_f32_e64 v8, |v176|, |v177|
	v_max_f32_e64 v9, |v134|, |v135|
	v_max3_f32 v8, |v180|, |v181|, v8
	v_max3_f32 v9, |v186|, |v187|, v9
	v_max3_f32 v7, v7, v8, v9
	v_max_f32_e64 v8, |v74|, |v75|
	v_max_f32_e64 v9, |v106|, |v107|
	v_max3_f32 v8, |v112|, |v113|, v8
	v_max3_f32 v9, |v108|, |v109|, v9
	v_max3_f32 v7, v7, v8, v9
	v_max_f32_e64 v8, |v110|, |v111|
	v_max_f32_e64 v9, |v44|, |v45|
	v_max3_f32 v8, |v120|, |v121|, v8
	v_max3_f32 v9, |v46|, |v47|, v9
	v_max3_f32 v7, v7, v8, v9
	v_max_f32_e64 v8, |v142|, |v143|
	v_max_f32_e64 v9, |v156|, |v157|
	v_max3_f32 v8, |v144|, |v145|, v8
	v_max3_f32 v9, |v158|, |v159|, v9
	v_max3_f32 v8, v8, 0, v9
	v_max_f32_e64 v9, |v104|, |v105|
	v_max3_f32 v9, |v162|, |v163|, v9
	v_max3_f32 v8, v8, v9, v10
	v_max_f32_e64 v9, |v60|, |v61|
	v_max_f32_e64 v10, |v90|, |v91|
	v_max3_f32 v9, |v68|, |v69|, v9
	v_max3_f32 v10, |v102|, |v103|, v10
	v_max3_f32 v8, v8, v9, v10
	v_max_f32_e64 v9, |v92|, |v93|
	v_max_f32_e64 v10, |v40|, |v41|
	v_max3_f32 v9, |v94|, |v95|, v9
	v_max3_f32 v10, |v42|, |v43|, v10
	v_max3_f32 v8, v8, v9, v10
	v_max_f32_e64 v9, |v136|, |v137|
	v_max_f32_e64 v10, |v146|, |v147|
	v_max3_f32 v9, |v138|, |v139|, v9
	v_max3_f32 v10, |v148|, |v149|, v10
	v_max3_f32 v9, v9, 0, v10
	v_max_f32_e64 v10, |v76|, |v77|
	v_max_f32_e64 v48, |v64|, |v65|
	v_max3_f32 v10, |v88|, |v89|, v10
	v_max3_f32 v48, |v66|, |v67|, v48
	v_max3_f32 v9, v9, v10, v48
	v_max_f32_e64 v10, |v56|, |v57|
	v_max_f32_e64 v48, |v62|, |v63|
	v_max3_f32 v10, |v58|, |v59|, v10
	v_max3_f32 v48, |v70|, |v71|, v48
	v_max3_f32 v9, v9, v10, v48
	v_max_f32_e64 v10, |v52|, |v53|
	v_max_f32_e64 v48, |v4|, |v5|
	v_max3_f32 v10, |v54|, |v55|, v10
	v_max3_f32 v48, |v2|, |v3|, v48
	v_max3_f32 v9, v9, v10, v48
	ds_bpermute_b32 v10, v167, v6
	s_waitcnt lgkmcnt(0)
	v_max_f32_e32 v10, v10, v10
	v_max_f32_e32 v6, v6, v10
	ds_bpermute_b32 v10, v169, v6
	s_waitcnt lgkmcnt(0)
	v_max_f32_e32 v10, v10, v10
	v_max_f32_e32 v6, v6, v10
	ds_bpermute_b32 v10, v213, v6
	s_waitcnt lgkmcnt(0)
	v_max_f32_e32 v10, v10, v10
	v_max_f32_e32 v6, v6, v10
	ds_bpermute_b32 v10, v214, v6
	s_waitcnt lgkmcnt(0)
	v_max_f32_e32 v10, v10, v10
	v_max_f32_e32 v6, v6, v10
	ds_bpermute_b32 v10, v215, v6
	s_waitcnt lgkmcnt(0)
	v_max_f32_e32 v10, v10, v10
	v_max_f32_e32 v6, v6, v10
	ds_bpermute_b32 v10, v216, v6
	s_waitcnt lgkmcnt(0)
	v_max_f32_e32 v10, v10, v10
	v_max_f32_e32 v10, v6, v10
	ds_bpermute_b32 v6, v167, v7
	s_waitcnt lgkmcnt(0)
	v_max_f32_e32 v6, v6, v6
	v_max_f32_e32 v6, v7, v6
	ds_bpermute_b32 v7, v169, v6
	s_waitcnt lgkmcnt(0)
	v_max_f32_e32 v7, v7, v7
	v_max_f32_e32 v6, v6, v7
	ds_bpermute_b32 v7, v213, v6
	s_waitcnt lgkmcnt(0)
	v_max_f32_e32 v7, v7, v7
	v_max_f32_e32 v6, v6, v7
	ds_bpermute_b32 v7, v214, v6
	s_waitcnt lgkmcnt(0)
	v_max_f32_e32 v7, v7, v7
	v_max_f32_e32 v6, v6, v7
	ds_bpermute_b32 v7, v215, v6
	s_waitcnt lgkmcnt(0)
	v_max_f32_e32 v7, v7, v7
	v_max_f32_e32 v48, v6, v7
	ds_bpermute_b32 v6, v167, v8
	ds_bpermute_b32 v49, v216, v48
	s_waitcnt lgkmcnt(1)
	v_max_f32_e32 v6, v6, v6
	v_max_f32_e32 v6, v8, v6
	ds_bpermute_b32 v8, v167, v9
	ds_bpermute_b32 v7, v169, v6
	s_waitcnt lgkmcnt(1)
	v_max_f32_e32 v8, v8, v8
	v_max_f32_e32 v8, v9, v8
	ds_bpermute_b32 v9, v169, v8
	s_waitcnt lgkmcnt(1)
	v_max_f32_e32 v7, v7, v7
	v_max_f32_e32 v6, v6, v7
	ds_bpermute_b32 v7, v213, v6
	s_waitcnt lgkmcnt(1)
	v_max_f32_e32 v9, v9, v9
	v_max_f32_e32 v8, v8, v9
	ds_bpermute_b32 v9, v213, v8
	s_waitcnt lgkmcnt(1)
	v_max_f32_e32 v7, v7, v7
	v_max_f32_e32 v6, v6, v7
	ds_bpermute_b32 v7, v214, v6
	s_waitcnt lgkmcnt(1)
	v_max_f32_e32 v9, v9, v9
	v_max_f32_e32 v8, v8, v9
	ds_bpermute_b32 v9, v214, v8
	s_waitcnt lgkmcnt(1)
	v_max_f32_e32 v7, v7, v7
	v_max_f32_e32 v6, v6, v7
	ds_bpermute_b32 v7, v215, v6
	s_waitcnt lgkmcnt(1)
	v_max_f32_e32 v9, v9, v9
	v_max_f32_e32 v8, v8, v9
	ds_bpermute_b32 v9, v215, v8
	s_waitcnt lgkmcnt(1)
	v_max_f32_e32 v7, v7, v7
	v_max_f32_e32 v6, v6, v7
	ds_bpermute_b32 v7, v216, v6
	s_waitcnt lgkmcnt(1)
	v_max_f32_e32 v9, v9, v9
	v_max_f32_e32 v8, v8, v9
	ds_bpermute_b32 v9, v216, v8
	s_and_saveexec_b64 s[0:1], s[38:39]
	s_cbranch_execz .LBB0_545
	s_add_u32 s8, s92, s6
	v_mul_f32_e32 v50, 0x3c010204, v10
	s_addc_u32 s9, s93, s7
	global_store_dword v11, v50, s[8:9]
